# v6 plus L2 prefetch-ahead touches of node i+2 weights
# baseline (speedup 1.0000x reference)
.LBB1_2:
	v_lshrrev_b32_e32 v151, 4, v137
	s_lshl_b64 s[6:7], s[2:3], 4
	v_cmp_eq_u32_e64 s[2:3], 1, v151
	s_waitcnt vmcnt(31)
	v_cvt_f16_f32_e32 v8, v8
	v_cmp_gt_u32_e32 vcc, 16, v137
	s_waitcnt vmcnt(29)
	v_cndmask_b32_e64 v116, 0, v116, s[2:3]
	s_waitcnt vmcnt(21)
	v_cndmask_b32_e64 v100, 0, v100, s[2:3]
	v_cmp_eq_u32_e64 s[0:1], 2, v151
	v_cndmask_b32_e64 v114, 0, v114, s[2:3]
	v_cndmask_b32_e64 v115, 0, v115, s[2:3]
	v_cndmask_b32_e32 v6, v116, v6, vcc
	v_cndmask_b32_e64 v116, 0, v117, s[2:3]
	v_cndmask_b32_e64 v108, 0, v108, s[2:3]
	v_cndmask_b32_e32 v26, v100, v26, vcc
	v_cvt_f16_f32_e32 v29, v29
	v_cndmask_b32_e64 v100, 0, v101, s[2:3]
	v_cndmask_b32_e32 v28, 0, v28, vcc
	v_cndmask_b32_e64 v152, 0, 1.0, s[0:1]
	v_cndmask_b32_e32 v114, v114, v120, vcc
	v_cndmask_b32_e32 v115, v115, v121, vcc
	v_cndmask_b32_e32 v7, v116, v7, vcc
	v_cndmask_b32_e64 v106, 0, v106, s[2:3]
	v_cndmask_b32_e64 v107, 0, v107, s[2:3]
	v_cndmask_b32_e32 v14, v108, v14, vcc
	v_cndmask_b32_e64 v108, 0, v109, s[2:3]
	v_cndmask_b32_e32 v27, v100, v27, vcc
	v_cvt_f16_f32_e32 v100, v28
	v_cndmask_b32_e32 v116, 0, v8, vcc
	v_cvt_pk_f16_f32 v8, v6, v7
	v_cvt_pk_f16_f32 v7, v114, v115
	v_cndmask_b32_e64 v114, v152, v140, s[2:3]
	v_cndmask_b32_e32 v106, v106, v112, vcc
	v_cndmask_b32_e32 v107, v107, v113, vcc
	v_cndmask_b32_e32 v15, v108, v15, vcc
	v_cndmask_b32_e64 v98, 0, v98, s[2:3]
	v_cndmask_b32_e64 v99, 0, v99, s[2:3]
	v_cndmask_b32_e32 v110, v114, v110, vcc
	v_cndmask_b32_e64 v114, 0, v141, s[2:3]
	v_cndmask_b32_e32 v108, 0, v16, vcc
	v_cvt_pk_f16_f32 v16, v14, v15
	v_cvt_pk_f16_f32 v15, v106, v107
	v_cndmask_b32_e64 v106, v152, v138, s[2:3]
	v_cndmask_b32_e32 v98, v98, v104, vcc
	v_cndmask_b32_e32 v99, v99, v105, vcc
	v_cndmask_b32_e32 v111, v114, v111, vcc
	v_cndmask_b32_e32 v102, v106, v102, vcc
	v_cndmask_b32_e64 v106, 0, v139, s[2:3]
	v_cndmask_b32_e32 v29, 0, v29, vcc
	v_cvt_pk_f16_f32 v28, v26, v27
	v_cvt_pk_f16_f32 v27, v98, v99
	v_lshlrev_b32_e32 v101, 10, v1
	v_bitop3_b32 v98, v151, v0, 3 bitop3:0x78
	v_lshl_add_u64 v[130:131], s[4:5], 0, v[130:131]
	v_cvt_f16_f32_e32 v4, v4
	v_cvt_pk_f16_f32 v14, v110, v111
	v_cndmask_b32_e32 v103, v106, v103, vcc
	v_pack_b32_f16 v29, v100, v29
	v_lshl_or_b32 v111, v98, 4, v101
	v_lshlrev_b32_e32 v100, 4, v1
	s_movk_i32 s4, 0xc0
	v_cndmask_b32_e64 v124, 0, v124, s[2:3]
	v_cvt_pk_f16_f32 v26, v102, v103
	v_and_b32_e32 v112, 0xc0, v100
	v_bitop3_b32 v100, v100, s4, v111 bitop3:0x26
	s_lshl_b32 s4, s20, 3
	v_lshrrev_b32_e32 v102, 5, v137
	v_lshrrev_b32_e32 v104, 1, v137
	v_cndmask_b32_e64 v122, 0, v122, s[2:3]
	v_cndmask_b32_e64 v123, 0, v123, s[2:3]
	v_cndmask_b32_e32 v2, v124, v2, vcc
	v_cvt_f16_f32_e32 v5, v5
	v_cndmask_b32_e64 v124, 0, v125, s[2:3]
	v_cvt_f16_f32_e32 v9, v9
	v_or_b32_e32 v103, s4, v102
	v_and_or_b32 v110, v104, 8, v101
	v_bitop3_b32 v101, s4, v1, v102 bitop3:0x36
	s_lshl_b32 s4, s20, 4
	v_cndmask_b32_e32 v122, v122, v128, vcc
	v_cndmask_b32_e32 v123, v123, v129, vcc
	v_cndmask_b32_e32 v3, v124, v3, vcc
	v_cndmask_b32_e32 v17, 0, v17, vcc
	v_lshlrev_b32_e32 v107, 4, v101
	v_bitop3_b32 v101, v103, v1, 2 bitop3:0x36
	s_add_i32 s4, s4, 0x10000
	v_bfe_u32 v0, v0, 4, 2
	v_cndmask_b32_e64 v144, v152, v144, s[2:3]
	v_cndmask_b32_e32 v124, 0, v4, vcc
	v_cvt_pk_f16_f32 v4, v2, v3
	v_cvt_pk_f16_f32 v3, v122, v123
	v_cndmask_b32_e64 v122, v152, v142, s[2:3]
	v_cvt_pk_f16_f32 v17, v108, v17
	s_movk_i32 s5, 0x80
	v_lshlrev_b32_e32 v108, 4, v101
	v_bitop3_b32 v101, v103, v1, 4 bitop3:0x36
	s_cmp_lt_u32 s22, 64
	v_lshlrev_b32_e32 v104, 5, v0
	v_lshlrev_b32_e32 v0, 6, v0
	v_cndmask_b32_e32 v126, v144, v126, vcc
	v_cndmask_b32_e64 v144, 0, v145, s[2:3]
	v_cndmask_b32_e32 v118, v122, v118, vcc
	v_cndmask_b32_e64 v122, 0, v143, s[2:3]
	v_bitop3_b32 v99, v112, s5, v111 bitop3:0x36
	v_lshlrev_b32_e32 v109, 4, v101
	v_bitop3_b32 v101, v103, v1, 6 bitop3:0x36
	v_lshl_or_b32 v105, s20, 8, v0
	v_mov_b32_e32 v0, 0x1ec00
	s_cselect_b64 s[4:5], -1, 0
	v_cndmask_b32_e32 v127, v144, v127, vcc
	v_cndmask_b32_e32 v5, 0, v5, vcc
	v_cndmask_b32_e32 v119, v122, v119, vcc
	v_cndmask_b32_e32 v9, 0, v9, vcc
	v_lshlrev_b32_e32 v113, 4, v101
	v_lshlrev_b32_e32 v101, 5, v1
	v_lshl_add_u32 v106, v137, 6, v0
	v_cndmask_b32_e64 v0, 0, 1, s[4:5]
	v_lshl_add_u64 v[132:133], s[8:9], 0, v[132:133]
	v_or_b32_e32 v148, 0x400, v147
	v_or_b32_e32 v149, 0x800, v147
	v_or_b32_e32 v150, 0xc00, v147
	v_cvt_pk_f16_f32 v2, v126, v127
	v_pack_b32_f16 v5, v124, v5
	v_cvt_pk_f16_f32 v6, v118, v119
	v_pack_b32_f16 v9, v116, v9
	v_bitop3_b32 v98, v112, 64, v111 bitop3:0x36
	v_lshl_or_b32 v104, s20, 7, v104
	s_mov_b32 s22, 0x98000
	s_mov_b32 s23, 0x5040100
	s_mov_b32 s24, 0x7060302
	v_add_u32_e32 v107, v107, v110
	v_add_u32_e32 v108, v108, v110
	v_add_u32_e32 v109, v109, v110
	v_add_u32_e32 v110, v113, v110
	v_add_u32_e32 v111, v112, v111
	v_lshlrev_b32_e32 v113, 4, v137
	v_or_b32_e32 v113, 0x10000, v113
	s_lshr_b32 s28, s20, 2
	s_and_b32 s29, s20, 3
	s_lshl_b32 s28, s28, 10
	s_lshl_b32 s29, s29, 2
	s_add_i32 s28, s28, s29
	v_add_u32_e32 v112, s28, v113
	v_cmp_eq_u32_e64 s[26:27], 3, v151
	v_add_u32_e32 v114, 0x12400, v101
	s_lshr_b32 s31, s6, 13
	s_and_b32 s31, s31, 31
	s_lshl_b32 s31, s31, 14
	s_lshl_b32 s33, s20, 11
	s_or_b32 s31, s31, s33
	v_lshl_or_b32 v116, v137, 5, s31
	s_mov_b32 s33, 0x80000
	buffer_load_dword v115, v116, s[16:19], s33 offen
	v_cmp_ne_u32_e64 s[4:5], 1, v0
	s_waitcnt vmcnt(16)
	v_cndmask_b32_e64 v1, v30, v134, s[0:1]
	v_bfi_b32 v30, s10, v1, v30
	v_perm_b32 v1, v22, v134, s24
	v_cndmask_b32_e64 v22, v22, v1, s[0:1]
	v_bfi_b32 v1, s10, v135, v18
	v_perm_b32 v121, v10, v135, s24
	v_cndmask_b32_e64 v18, v18, v1, s[0:1]
	v_cndmask_b32_e64 v10, v10, v121, s[0:1]
	v_mov_b32_e32 v121, v136
	v_mov_b32_e32 v144, v136
	v_mov_b32_e32 v145, v136
	v_mov_b32_e32 v0, v136
	v_mov_b32_e32 v1, v136
	s_waitcnt lgkmcnt(0)
	s_barrier
	ds_read_u16 v248, v114
	ds_read_u16 v249, v114 offset:512
	ds_read_u16 v250, v114 offset:1024
	ds_read_u16 v251, v114 offset:1536
	v_add_u32_e32 v114, 2, v114
	s_branch .LBB1_4

.LBB1_4:
	s_waitcnt lgkmcnt(0)
	s_and_saveexec_b64 s[8:9], s[2:3]
	v_perm_b32 v5, v1, v248, s23
	v_perm_b32 v9, v121, v249, s23
	v_perm_b32 v17, v144, v250, s23
	v_perm_b32 v29, v145, v251, s23
	s_or_b64 exec, exec, s[8:9]
	v_add_u32_e32 v0, 0x12c00, v105
	ds_read_b128 v[240:243], v0
	ds_read_b128 v[244:247], v0 offset:16
	ds_read_b128 v[248:251], v0 offset:32
	ds_read_b128 v[252:255], v0 offset:48
	v_mfma_f32_16x16x32_f16 v[126:129], v[30:33], v[6:9], 0
	s_cmp_lg_u32 s22, 0x818000
	v_mfma_f32_16x16x32_f16 v[122:125], v[30:33], v[2:5], 0
	s_cselect_b32 s9, s11, 15
	s_nop 2
	v_cvt_pk_f16_f32 v121, v126, v127
	v_cvt_pk_f16_f32 v127, v128, v129
	v_mfma_f32_16x16x32_f16 v[134:137], v[30:33], v[14:17], 0
	v_pk_max_f16 v126, v121, 0
	s_nop 0
	v_cvt_pk_f16_f32 v0, v122, v123
	v_cvt_pk_f16_f32 v1, v124, v125
	v_mfma_f32_16x16x32_f16 v[30:33], v[30:33], v[26:29], 0
	v_pk_max_f16 v127, v127, 0
	v_pk_max_f16 v0, v0, 0
	v_pk_max_f16 v1, v1, 0
	v_mfma_f32_16x16x32_f16 v[122:125], v[22:25], v[2:5], 0
	ds_write2st64_b64 v107, v[0:1], v[126:127] offset1:32
	s_nop 1
	v_cvt_pk_f16_f32 v0, v134, v135
	v_cvt_pk_f16_f32 v1, v136, v137
	v_mfma_f32_16x16x32_f16 v[126:129], v[22:25], v[6:9], 0
	s_nop 0
	v_cvt_pk_f16_f32 v30, v30, v31
	v_cvt_pk_f16_f32 v31, v32, v33
	v_pk_max_f16 v0, v0, 0
	v_mfma_f32_16x16x32_f16 v[134:137], v[22:25], v[14:17], 0
	v_pk_max_f16 v30, v30, 0
	v_pk_max_f16 v31, v31, 0
	v_pk_max_f16 v1, v1, 0
	v_mfma_f32_16x16x32_f16 v[22:25], v[22:25], v[26:29], 0
	ds_write2st64_b64 v107, v[0:1], v[30:31] offset0:64 offset1:96
	v_cvt_pk_f16_f32 v0, v122, v123
	v_cvt_pk_f16_f32 v1, v124, v125
	v_mfma_f32_16x16x32_f16 v[30:33], v[18:21], v[2:5], 0
	v_pk_max_f16 v0, v0, 0
	v_cvt_pk_f16_f32 v139, v128, v129
	v_pk_max_f16 v1, v1, 0
	v_mfma_f32_16x16x32_f16 v[122:125], v[18:21], v[6:9], 0
	v_cvt_pk_f16_f32 v121, v126, v127
	v_pk_max_f16 v138, v121, 0
	v_pk_max_f16 v139, v139, 0
	v_mfma_f32_16x16x32_f16 v[126:129], v[18:21], v[14:17], 0
	ds_write2st64_b64 v108, v[0:1], v[138:139] offset1:32
	v_cvt_pk_f16_f32 v0, v134, v135
	v_cvt_pk_f16_f32 v1, v136, v137
	v_mfma_f32_16x16x32_f16 v[18:21], v[18:21], v[26:29], 0
	v_pk_max_f16 v0, v0, 0
	v_cvt_pk_f16_f32 v139, v24, v25
	v_pk_max_f16 v1, v1, 0
	v_mfma_f32_16x16x32_f16 v[134:137], v[10:13], v[2:5], 0
	v_cvt_pk_f16_f32 v121, v22, v23
	v_pk_max_f16 v138, v121, 0
	v_pk_max_f16 v139, v139, 0
	ds_write2st64_b64 v108, v[0:1], v[138:139] offset0:64 offset1:96
	v_cvt_pk_f16_f32 v0, v30, v31
	v_mfma_f32_16x16x32_f16 v[22:25], v[10:13], v[6:9], 0
	v_cvt_pk_f16_f32 v1, v32, v33
	v_pk_max_f16 v0, v0, 0
	v_cvt_pk_f16_f32 v30, v122, v123
	v_cvt_pk_f16_f32 v31, v124, v125
	v_mfma_f32_16x16x32_f16 v[138:141], v[10:13], v[14:17], 0
	v_pk_max_f16 v1, v1, 0
	v_pk_max_f16 v30, v30, 0
	v_pk_max_f16 v31, v31, 0
	ds_write2st64_b64 v109, v[0:1], v[30:31] offset1:32
	v_cvt_pk_f16_f32 v0, v126, v127
	v_mfma_f32_16x16x32_f16 v[10:13], v[10:13], v[26:29], 0
	v_cvt_pk_f16_f32 v1, v128, v129
	v_pk_max_f16 v0, v0, 0
	v_cvt_pk_f16_f32 v18, v18, v19
	v_cvt_pk_f16_f32 v19, v20, v21
	v_pk_max_f16 v1, v1, 0
	v_pk_max_f16 v18, v18, 0
	v_pk_max_f16 v19, v19, 0
	ds_write2st64_b64 v109, v[0:1], v[18:19] offset0:64 offset1:96
	v_cvt_pk_f16_f32 v0, v134, v135
	v_cvt_pk_f16_f32 v1, v136, v137
	v_pk_max_f16 v0, v0, 0
	v_cvt_pk_f16_f32 v18, v22, v23
	v_cvt_pk_f16_f32 v19, v24, v25
	v_pk_max_f16 v1, v1, 0
	v_pk_max_f16 v18, v18, 0
	v_pk_max_f16 v19, v19, 0
	ds_write2st64_b64 v110, v[0:1], v[18:19] offset1:32
	v_cvt_pk_f16_f32 v0, v138, v139
	v_cvt_pk_f16_f32 v1, v140, v141
	v_pk_max_f16 v0, v0, 0
	v_cvt_pk_f16_f32 v10, v10, v11
	v_cvt_pk_f16_f32 v11, v12, v13
	v_pk_max_f16 v1, v1, 0
	v_pk_max_f16 v10, v10, 0
	v_pk_max_f16 v11, v11, 0
	ds_write2st64_b64 v110, v[0:1], v[10:11] offset0:64 offset1:96
	s_waitcnt lgkmcnt(0)
	s_barrier
	ds_read_b128 v[122:125], v111
	ds_read_b128 v[126:129], v111 offset:16384
	ds_read_b128 v[134:137], v111 offset:32768
	ds_read_b128 v[138:141], v111 offset:49152
	ds_read_b128 v[142:145], v98
	ds_read_b128 v[152:155], v98 offset:16384
	ds_read_b128 v[156:159], v98 offset:32768
	ds_read_b128 v[160:163], v98 offset:49152
	s_lshl_b32 s20, s9, 7
	v_lshl_add_u64 v[0:1], s[20:21], 3, v[132:133]
	s_add_i32 s25, s22, 0xfff88000
	s_lshl_b32 s8, s9, 8
	buffer_load_dwordx4 v[192:195], v147, s[16:19], s25 offen
	buffer_load_dwordx4 v[196:199], v148, s[16:19], s25 offen
	buffer_load_dwordx4 v[200:203], v149, s[16:19], s25 offen
	buffer_load_dwordx4 v[204:207], v150, s[16:19], s25 offen
	s_waitcnt vmcnt(20) lgkmcnt(7)
	v_mfma_f32_16x16x32_f16 v[164:167], v[58:61], v[122:125], v[240:243]
	s_waitcnt lgkmcnt(6)
	v_mfma_f32_16x16x32_f16 v[168:171], v[58:61], v[126:129], v[240:243]
	s_waitcnt lgkmcnt(5)
	v_mfma_f32_16x16x32_f16 v[172:175], v[58:61], v[134:137], v[240:243]
	s_waitcnt lgkmcnt(4)
	v_mfma_f32_16x16x32_f16 v[10:13], v[58:61], v[138:141], v[240:243]
	s_waitcnt vmcnt(19)
	v_mfma_f32_16x16x32_f16 v[58:61], v[54:57], v[122:125], v[244:247]
	v_mfma_f32_16x16x32_f16 v[176:179], v[54:57], v[126:129], v[244:247]
	v_mfma_f32_16x16x32_f16 v[180:183], v[54:57], v[134:137], v[244:247]
	v_mfma_f32_16x16x32_f16 v[18:21], v[54:57], v[138:141], v[244:247]
	s_waitcnt vmcnt(18)
	v_mfma_f32_16x16x32_f16 v[54:57], v[50:53], v[122:125], v[248:251]
	v_mfma_f32_16x16x32_f16 v[184:187], v[50:53], v[126:129], v[248:251]
	v_mfma_f32_16x16x32_f16 v[188:191], v[50:53], v[134:137], v[248:251]
	v_mfma_f32_16x16x32_f16 v[22:25], v[50:53], v[138:141], v[248:251]
	s_waitcnt vmcnt(17)
	v_mfma_f32_16x16x32_f16 v[50:53], v[38:41], v[122:125], v[252:255]
	v_mfma_f32_16x16x32_f16 v[122:125], v[38:41], v[126:129], v[252:255]
	v_mfma_f32_16x16x32_f16 v[126:129], v[38:41], v[134:137], v[252:255]
	v_mfma_f32_16x16x32_f16 v[38:41], v[38:41], v[138:141], v[252:255]
	ds_read_b128 v[136:139], v99
	ds_read_b128 v[208:211], v99 offset:16384
	ds_read_b128 v[212:215], v99 offset:32768
	ds_read_b128 v[216:219], v99 offset:49152
	s_add_i32 s9, s22, 0xfff90000
	s_waitcnt vmcnt(16) lgkmcnt(7)
	v_mfma_f32_16x16x32_f16 v[164:167], v[94:97], v[142:145], v[164:167]
	s_waitcnt lgkmcnt(6)
	v_mfma_f32_16x16x32_f16 v[168:171], v[94:97], v[152:155], v[168:171]
	s_waitcnt vmcnt(15)
	v_mfma_f32_16x16x32_f16 v[58:61], v[90:93], v[142:145], v[58:61]
	v_mfma_f32_16x16x32_f16 v[176:179], v[90:93], v[152:155], v[176:179]
	s_waitcnt vmcnt(14)
	v_mfma_f32_16x16x32_f16 v[54:57], v[78:81], v[142:145], v[54:57]
	v_mfma_f32_16x16x32_f16 v[184:187], v[78:81], v[152:155], v[184:187]
	s_waitcnt vmcnt(13)
	v_mfma_f32_16x16x32_f16 v[50:53], v[34:37], v[142:145], v[50:53]
	buffer_load_dwordx4 v[140:143], v147, s[16:19], s9 offen
	buffer_load_dwordx4 v[220:223], v148, s[16:19], s9 offen
	v_mfma_f32_16x16x32_f16 v[122:125], v[34:37], v[152:155], v[122:125]
	buffer_load_dwordx4 v[152:155], v149, s[16:19], s9 offen
	buffer_load_dwordx4 v[224:227], v150, s[16:19], s9 offen
	s_mov_b32 s9, s21
	s_waitcnt lgkmcnt(5)
	v_mfma_f32_16x16x32_f16 v[172:175], v[94:97], v[156:159], v[172:175]
	s_waitcnt lgkmcnt(4)
	v_mfma_f32_16x16x32_f16 v[94:97], v[94:97], v[160:163], v[10:13]
	s_nop 2
	v_lshl_add_u64 v[10:11], s[8:9], 4, v[130:131]
	v_mfma_f32_16x16x32_f16 v[180:183], v[90:93], v[156:159], v[180:183]
	v_mfma_f32_16x16x32_f16 v[90:93], v[90:93], v[160:163], v[18:21]
	v_mfma_f32_16x16x32_f16 v[188:191], v[78:81], v[156:159], v[188:191]
	v_mfma_f32_16x16x32_f16 v[78:81], v[78:81], v[160:163], v[22:25]
	global_load_dwordx4 v[30:33], v[10:11], off
	s_nop 1
	global_load_dwordx4 v[22:25], v[10:11], off offset:1024
	global_load_dwordx4 v[18:21], v[10:11], off offset:2048
	s_nop 0
	global_load_dwordx4 v[10:13], v[10:11], off offset:3072
	s_nop 0
	global_load_dwordx2 v[134:135], v[0:1], off
	v_mfma_f32_16x16x32_f16 v[126:129], v[34:37], v[156:159], v[126:129]
	v_mfma_f32_16x16x32_f16 v[34:37], v[34:37], v[160:163], v[38:41]
	s_nop 2
	ds_read_b128 v[38:41], v100
	ds_read_b128 v[156:159], v100 offset:16384
	ds_read_b128 v[160:163], v100 offset:32768
	ds_read_b128 v[228:231], v100 offset:49152
	s_add_i32 s8, s22, 0xfff98000
	s_waitcnt vmcnt(21) lgkmcnt(7)
	v_mfma_f32_16x16x32_f16 v[164:167], v[82:85], v[136:139], v[164:167]
	s_waitcnt lgkmcnt(6)
	v_mfma_f32_16x16x32_f16 v[168:171], v[82:85], v[208:211], v[168:171]
	s_waitcnt lgkmcnt(5)
	v_mfma_f32_16x16x32_f16 v[172:175], v[82:85], v[212:215], v[172:175]
	s_waitcnt lgkmcnt(4)
	v_mfma_f32_16x16x32_f16 v[82:85], v[82:85], v[216:219], v[94:97]
	s_waitcnt vmcnt(20)
	v_mfma_f32_16x16x32_f16 v[58:61], v[70:73], v[136:139], v[58:61]
	v_mfma_f32_16x16x32_f16 v[94:97], v[70:73], v[208:211], v[176:179]
	v_mfma_f32_16x16x32_f16 v[176:179], v[70:73], v[212:215], v[180:183]
	v_mfma_f32_16x16x32_f16 v[70:73], v[70:73], v[216:219], v[90:93]
	s_waitcnt vmcnt(19)
	v_mfma_f32_16x16x32_f16 v[54:57], v[62:65], v[136:139], v[54:57]
	v_mfma_f32_16x16x32_f16 v[90:93], v[62:65], v[208:211], v[184:187]
	v_mfma_f32_16x16x32_f16 v[180:183], v[62:65], v[212:215], v[188:191]
	v_mfma_f32_16x16x32_f16 v[62:65], v[62:65], v[216:219], v[78:81]
	s_waitcnt vmcnt(18)
	v_mfma_f32_16x16x32_f16 v[50:53], v[42:45], v[136:139], v[50:53]
	v_mfma_f32_16x16x32_f16 v[78:81], v[42:45], v[208:211], v[122:125]
	v_mfma_f32_16x16x32_f16 v[122:125], v[42:45], v[212:215], v[126:129]
	s_nop 2
	buffer_load_dwordx4 v[126:129], v147, s[16:19], s8 offen
	buffer_load_dwordx4 v[136:139], v148, s[16:19], s8 offen
	buffer_load_dwordx4 v[184:187], v149, s[16:19], s8 offen
	buffer_load_dwordx4 v[188:191], v150, s[16:19], s8 offen
	v_mfma_f32_16x16x32_f16 v[34:37], v[42:45], v[216:219], v[34:37]
	ds_read_b128 v[42:45], v111 offset:256
	ds_read_b128 v[208:211], v111 offset:16640
	ds_read_b128 v[212:215], v111 offset:33024
	ds_read_b128 v[216:219], v111 offset:49408
	s_add_i32 s8, s22, 0xfffa0000
	s_waitcnt vmcnt(21) lgkmcnt(7)
	v_mfma_f32_16x16x32_f16 v[164:167], v[86:89], v[38:41], v[164:167]
	s_waitcnt lgkmcnt(6)
	v_mfma_f32_16x16x32_f16 v[168:171], v[86:89], v[156:159], v[168:171]
	s_waitcnt lgkmcnt(5)
	v_mfma_f32_16x16x32_f16 v[172:175], v[86:89], v[160:163], v[172:175]
	s_waitcnt lgkmcnt(4)
	v_mfma_f32_16x16x32_f16 v[82:85], v[86:89], v[228:231], v[82:85]
	s_waitcnt vmcnt(20)
	v_mfma_f32_16x16x32_f16 v[58:61], v[74:77], v[38:41], v[58:61]
	v_mfma_f32_16x16x32_f16 v[86:89], v[74:77], v[156:159], v[94:97]
	v_mfma_f32_16x16x32_f16 v[94:97], v[74:77], v[160:163], v[176:179]
	v_mfma_f32_16x16x32_f16 v[70:73], v[74:77], v[228:231], v[70:73]
	s_waitcnt vmcnt(19)
	v_mfma_f32_16x16x32_f16 v[54:57], v[66:69], v[38:41], v[54:57]
	v_mfma_f32_16x16x32_f16 v[74:77], v[66:69], v[156:159], v[90:93]
	v_mfma_f32_16x16x32_f16 v[90:93], v[66:69], v[160:163], v[180:183]
	v_mfma_f32_16x16x32_f16 v[62:65], v[66:69], v[228:231], v[62:65]
	s_waitcnt vmcnt(18)
	v_mfma_f32_16x16x32_f16 v[38:41], v[46:49], v[38:41], v[50:53]
	v_mfma_f32_16x16x32_f16 v[50:53], v[46:49], v[156:159], v[78:81]
	v_mfma_f32_16x16x32_f16 v[66:69], v[46:49], v[160:163], v[122:125]
	s_nop 1
	buffer_load_dwordx4 v[78:81], v147, s[16:19], s8 offen
	buffer_load_dwordx4 v[122:125], v148, s[16:19], s8 offen
	buffer_load_dwordx4 v[156:159], v149, s[16:19], s8 offen
	buffer_load_dwordx4 v[160:163], v150, s[16:19], s8 offen
	v_mfma_f32_16x16x32_f16 v[34:37], v[46:49], v[228:231], v[34:37]
	ds_read_b128 v[46:49], v98 offset:256
	ds_read_b128 v[176:179], v98 offset:16640
	ds_read_b128 v[180:183], v98 offset:33024
	ds_read_b128 v[228:231], v98 offset:49408
	s_add_i32 s8, s22, 0xfffa8000
	s_waitcnt vmcnt(20) lgkmcnt(7)
	v_mfma_f32_16x16x32_f16 v[164:167], v[192:195], v[42:45], v[164:167]
	s_waitcnt lgkmcnt(6)
	v_mfma_f32_16x16x32_f16 v[168:171], v[192:195], v[208:211], v[168:171]
	s_waitcnt lgkmcnt(5)
	v_mfma_f32_16x16x32_f16 v[172:175], v[192:195], v[212:215], v[172:175]
	s_waitcnt lgkmcnt(4)
	v_mfma_f32_16x16x32_f16 v[82:85], v[192:195], v[216:219], v[82:85]
	s_waitcnt vmcnt(19)
	v_mfma_f32_16x16x32_f16 v[58:61], v[196:199], v[42:45], v[58:61]
	v_mfma_f32_16x16x32_f16 v[86:89], v[196:199], v[208:211], v[86:89]
	v_mfma_f32_16x16x32_f16 v[94:97], v[196:199], v[212:215], v[94:97]
	v_mfma_f32_16x16x32_f16 v[70:73], v[196:199], v[216:219], v[70:73]
	s_waitcnt vmcnt(18)
	v_mfma_f32_16x16x32_f16 v[54:57], v[200:203], v[42:45], v[54:57]
	v_mfma_f32_16x16x32_f16 v[74:77], v[200:203], v[208:211], v[74:77]
	v_mfma_f32_16x16x32_f16 v[90:93], v[200:203], v[212:215], v[90:93]
	v_mfma_f32_16x16x32_f16 v[62:65], v[200:203], v[216:219], v[62:65]
	s_waitcnt vmcnt(17)
	v_mfma_f32_16x16x32_f16 v[38:41], v[204:207], v[42:45], v[38:41]
	v_mfma_f32_16x16x32_f16 v[42:45], v[204:207], v[208:211], v[50:53]
	v_mfma_f32_16x16x32_f16 v[50:53], v[204:207], v[212:215], v[66:69]
	s_nop 2
	buffer_load_dwordx4 v[66:69], v147, s[16:19], s8 offen
	buffer_load_dwordx4 v[192:195], v148, s[16:19], s8 offen
	buffer_load_dwordx4 v[196:199], v149, s[16:19], s8 offen
	buffer_load_dwordx4 v[200:203], v150, s[16:19], s8 offen
	v_mfma_f32_16x16x32_f16 v[34:37], v[204:207], v[216:219], v[34:37]
	ds_read_b128 v[204:207], v99 offset:256
	ds_read_b128 v[208:211], v99 offset:16640
	ds_read_b128 v[212:215], v99 offset:33024
	ds_read_b128 v[216:219], v99 offset:49408
	s_add_i32 s8, s22, 0xfffb0000
	s_waitcnt vmcnt(20) lgkmcnt(7)
	v_mfma_f32_16x16x32_f16 v[164:167], v[140:143], v[46:49], v[164:167]
	s_waitcnt lgkmcnt(6)
	v_mfma_f32_16x16x32_f16 v[168:171], v[140:143], v[176:179], v[168:171]
	s_waitcnt lgkmcnt(5)
	v_mfma_f32_16x16x32_f16 v[172:175], v[140:143], v[180:183], v[172:175]
	s_waitcnt lgkmcnt(4)
	v_mfma_f32_16x16x32_f16 v[82:85], v[140:143], v[228:231], v[82:85]
	s_waitcnt vmcnt(19)
	v_mfma_f32_16x16x32_f16 v[58:61], v[220:223], v[46:49], v[58:61]
	v_mfma_f32_16x16x32_f16 v[86:89], v[220:223], v[176:179], v[86:89]
	s_waitcnt vmcnt(18)
	v_mfma_f32_16x16x32_f16 v[54:57], v[152:155], v[46:49], v[54:57]
	v_mfma_f32_16x16x32_f16 v[74:77], v[152:155], v[176:179], v[74:77]
	v_mfma_f32_16x16x32_f16 v[90:93], v[152:155], v[180:183], v[90:93]
	v_mfma_f32_16x16x32_f16 v[62:65], v[152:155], v[228:231], v[62:65]
	s_waitcnt vmcnt(17)
	v_mfma_f32_16x16x32_f16 v[38:41], v[224:227], v[46:49], v[38:41]
	v_mfma_f32_16x16x32_f16 v[42:45], v[224:227], v[176:179], v[42:45]
	v_mfma_f32_16x16x32_f16 v[46:49], v[224:227], v[180:183], v[50:53]
	s_nop 2
	buffer_load_dwordx4 v[50:53], v147, s[16:19], s8 offen
	buffer_load_dwordx4 v[140:143], v148, s[16:19], s8 offen
	buffer_load_dwordx4 v[152:155], v149, s[16:19], s8 offen
	buffer_load_dwordx4 v[176:179], v150, s[16:19], s8 offen
	v_mfma_f32_16x16x32_f16 v[94:97], v[220:223], v[180:183], v[94:97]
	v_mfma_f32_16x16x32_f16 v[70:73], v[220:223], v[228:231], v[70:73]
	v_mfma_f32_16x16x32_f16 v[34:37], v[224:227], v[228:231], v[34:37]
	ds_read_b128 v[180:183], v100 offset:256
	ds_read_b128 v[220:223], v100 offset:16640
	ds_read_b128 v[224:227], v100 offset:33024
	ds_read_b128 v[228:231], v100 offset:49408
	s_add_i32 s8, s22, 0xfffb8000
	s_waitcnt vmcnt(15) lgkmcnt(7)
	v_mfma_f32_16x16x32_f16 v[164:167], v[126:129], v[204:207], v[164:167]
	s_waitcnt lgkmcnt(6)
	v_mfma_f32_16x16x32_f16 v[168:171], v[126:129], v[208:211], v[168:171]
	s_waitcnt lgkmcnt(5)
	v_mfma_f32_16x16x32_f16 v[172:175], v[126:129], v[212:215], v[172:175]
	s_waitcnt lgkmcnt(4)
	v_mfma_f32_16x16x32_f16 v[82:85], v[126:129], v[216:219], v[82:85]
	s_waitcnt vmcnt(14)
	v_mfma_f32_16x16x32_f16 v[58:61], v[136:139], v[204:207], v[58:61]
	v_mfma_f32_16x16x32_f16 v[86:89], v[136:139], v[208:211], v[86:89]
	v_mfma_f32_16x16x32_f16 v[94:97], v[136:139], v[212:215], v[94:97]
	v_mfma_f32_16x16x32_f16 v[70:73], v[136:139], v[216:219], v[70:73]
	s_waitcnt vmcnt(13)
	v_mfma_f32_16x16x32_f16 v[54:57], v[184:187], v[204:207], v[54:57]
	v_mfma_f32_16x16x32_f16 v[74:77], v[184:187], v[208:211], v[74:77]
	v_mfma_f32_16x16x32_f16 v[90:93], v[184:187], v[212:215], v[90:93]
	v_mfma_f32_16x16x32_f16 v[62:65], v[184:187], v[216:219], v[62:65]
	s_waitcnt vmcnt(12)
	v_mfma_f32_16x16x32_f16 v[38:41], v[188:191], v[204:207], v[38:41]
	buffer_load_dwordx4 v[126:129], v147, s[16:19], s8 offen
	buffer_load_dwordx4 v[136:139], v148, s[16:19], s8 offen
	buffer_load_dwordx4 v[184:187], v149, s[16:19], s8 offen
	buffer_load_dwordx4 v[204:207], v150, s[16:19], s8 offen
	v_mfma_f32_16x16x32_f16 v[42:45], v[188:191], v[208:211], v[42:45]
	v_mfma_f32_16x16x32_f16 v[46:49], v[188:191], v[212:215], v[46:49]
	v_mfma_f32_16x16x32_f16 v[34:37], v[188:191], v[216:219], v[34:37]
	ds_read_b128 v[188:191], v111 offset:512
	ds_read_b128 v[208:211], v111 offset:16896
	ds_read_b128 v[212:215], v111 offset:33280
	ds_read_b128 v[216:219], v111 offset:49664
	s_add_i32 s8, s22, 0xfffc0000
	s_waitcnt vmcnt(15) lgkmcnt(7)
	v_mfma_f32_16x16x32_f16 v[164:167], v[78:81], v[180:183], v[164:167]
	s_waitcnt lgkmcnt(6)
	v_mfma_f32_16x16x32_f16 v[168:171], v[78:81], v[220:223], v[168:171]
	s_waitcnt lgkmcnt(5)
	v_mfma_f32_16x16x32_f16 v[172:175], v[78:81], v[224:227], v[172:175]
	s_waitcnt lgkmcnt(4)
	v_mfma_f32_16x16x32_f16 v[78:81], v[78:81], v[228:231], v[82:85]
	s_waitcnt vmcnt(14)
	v_mfma_f32_16x16x32_f16 v[58:61], v[122:125], v[180:183], v[58:61]
	v_mfma_f32_16x16x32_f16 v[82:85], v[122:125], v[220:223], v[86:89]
	v_mfma_f32_16x16x32_f16 v[86:89], v[122:125], v[224:227], v[94:97]
	v_mfma_f32_16x16x32_f16 v[70:73], v[122:125], v[228:231], v[70:73]
	s_waitcnt vmcnt(13)
	v_mfma_f32_16x16x32_f16 v[54:57], v[156:159], v[180:183], v[54:57]
	v_mfma_f32_16x16x32_f16 v[74:77], v[156:159], v[220:223], v[74:77]
	v_mfma_f32_16x16x32_f16 v[90:93], v[156:159], v[224:227], v[90:93]
	v_mfma_f32_16x16x32_f16 v[62:65], v[156:159], v[228:231], v[62:65]
	s_waitcnt vmcnt(12)
	v_mfma_f32_16x16x32_f16 v[38:41], v[160:163], v[180:183], v[38:41]
	buffer_load_dwordx4 v[94:97], v147, s[16:19], s8 offen
	buffer_load_dwordx4 v[122:125], v148, s[16:19], s8 offen
	buffer_load_dwordx4 v[156:159], v149, s[16:19], s8 offen
	buffer_load_dwordx4 v[180:183], v150, s[16:19], s8 offen
	v_mfma_f32_16x16x32_f16 v[42:45], v[160:163], v[220:223], v[42:45]
	v_mfma_f32_16x16x32_f16 v[46:49], v[160:163], v[224:227], v[46:49]
	v_mfma_f32_16x16x32_f16 v[34:37], v[160:163], v[228:231], v[34:37]
	ds_read_b128 v[160:163], v98 offset:512
	ds_read_b128 v[220:223], v98 offset:16896
	ds_read_b128 v[224:227], v98 offset:33280
	ds_read_b128 v[228:231], v98 offset:49664
	s_add_i32 s8, s22, 0xfffc8000
	s_waitcnt vmcnt(15) lgkmcnt(7)
	v_mfma_f32_16x16x32_f16 v[164:167], v[66:69], v[188:191], v[164:167]
	s_waitcnt lgkmcnt(6)
	v_mfma_f32_16x16x32_f16 v[168:171], v[66:69], v[208:211], v[168:171]
	s_waitcnt lgkmcnt(5)
	v_mfma_f32_16x16x32_f16 v[172:175], v[66:69], v[212:215], v[172:175]
	s_waitcnt lgkmcnt(4)
	v_mfma_f32_16x16x32_f16 v[66:69], v[66:69], v[216:219], v[78:81]
	s_waitcnt vmcnt(14)
	v_mfma_f32_16x16x32_f16 v[58:61], v[192:195], v[188:191], v[58:61]
	v_mfma_f32_16x16x32_f16 v[78:81], v[192:195], v[208:211], v[82:85]
	v_mfma_f32_16x16x32_f16 v[82:85], v[192:195], v[212:215], v[86:89]
	v_mfma_f32_16x16x32_f16 v[70:73], v[192:195], v[216:219], v[70:73]
	s_waitcnt vmcnt(13)
	v_mfma_f32_16x16x32_f16 v[54:57], v[196:199], v[188:191], v[54:57]
	v_mfma_f32_16x16x32_f16 v[74:77], v[196:199], v[208:211], v[74:77]
	v_mfma_f32_16x16x32_f16 v[86:89], v[196:199], v[212:215], v[90:93]
	v_mfma_f32_16x16x32_f16 v[62:65], v[196:199], v[216:219], v[62:65]
	s_waitcnt vmcnt(12)
	v_mfma_f32_16x16x32_f16 v[38:41], v[200:203], v[188:191], v[38:41]
	buffer_load_dwordx4 v[90:93], v147, s[16:19], s8 offen
	buffer_load_dwordx4 v[188:191], v148, s[16:19], s8 offen
	buffer_load_dwordx4 v[192:195], v149, s[16:19], s8 offen
	buffer_load_dwordx4 v[196:199], v150, s[16:19], s8 offen
	v_mfma_f32_16x16x32_f16 v[42:45], v[200:203], v[208:211], v[42:45]
	v_mfma_f32_16x16x32_f16 v[46:49], v[200:203], v[212:215], v[46:49]
	v_mfma_f32_16x16x32_f16 v[34:37], v[200:203], v[216:219], v[34:37]
	ds_read_b128 v[200:203], v99 offset:512
	ds_read_b128 v[208:211], v99 offset:16896
	ds_read_b128 v[212:215], v99 offset:33280
	ds_read_b128 v[216:219], v99 offset:49664
	s_add_i32 s8, s22, 0xfffd0000
	s_waitcnt vmcnt(15) lgkmcnt(7)
	v_mfma_f32_16x16x32_f16 v[164:167], v[50:53], v[160:163], v[164:167]
	s_waitcnt lgkmcnt(6)
	v_mfma_f32_16x16x32_f16 v[168:171], v[50:53], v[220:223], v[168:171]
	s_waitcnt lgkmcnt(5)
	v_mfma_f32_16x16x32_f16 v[172:175], v[50:53], v[224:227], v[172:175]
	s_waitcnt lgkmcnt(4)
	v_mfma_f32_16x16x32_f16 v[50:53], v[50:53], v[228:231], v[66:69]
	s_waitcnt vmcnt(14)
	v_mfma_f32_16x16x32_f16 v[58:61], v[140:143], v[160:163], v[58:61]
	v_mfma_f32_16x16x32_f16 v[66:69], v[140:143], v[220:223], v[78:81]
	v_mfma_f32_16x16x32_f16 v[78:81], v[140:143], v[224:227], v[82:85]
	v_mfma_f32_16x16x32_f16 v[70:73], v[140:143], v[228:231], v[70:73]
	s_waitcnt vmcnt(13)
	v_mfma_f32_16x16x32_f16 v[54:57], v[152:155], v[160:163], v[54:57]
	v_mfma_f32_16x16x32_f16 v[74:77], v[152:155], v[220:223], v[74:77]
	v_mfma_f32_16x16x32_f16 v[82:85], v[152:155], v[224:227], v[86:89]
	v_mfma_f32_16x16x32_f16 v[62:65], v[152:155], v[228:231], v[62:65]
	s_waitcnt vmcnt(12)
	v_mfma_f32_16x16x32_f16 v[38:41], v[176:179], v[160:163], v[38:41]
	buffer_load_dwordx4 v[86:89], v147, s[16:19], s8 offen
	buffer_load_dwordx4 v[140:143], v148, s[16:19], s8 offen
	buffer_load_dwordx4 v[152:155], v149, s[16:19], s8 offen
	buffer_load_dwordx4 v[160:163], v150, s[16:19], s8 offen
	v_mfma_f32_16x16x32_f16 v[42:45], v[176:179], v[220:223], v[42:45]
	v_mfma_f32_16x16x32_f16 v[46:49], v[176:179], v[224:227], v[46:49]
	v_mfma_f32_16x16x32_f16 v[34:37], v[176:179], v[228:231], v[34:37]
	ds_read_b128 v[176:179], v100 offset:512
	ds_read_b128 v[220:223], v100 offset:16896
	ds_read_b128 v[224:227], v100 offset:33280
	ds_read_b128 v[228:231], v100 offset:49664
	s_add_i32 s8, s22, 0xfffd8000
	s_waitcnt vmcnt(15) lgkmcnt(7)
	v_mfma_f32_16x16x32_f16 v[164:167], v[126:129], v[200:203], v[164:167]
	s_waitcnt lgkmcnt(6)
	v_mfma_f32_16x16x32_f16 v[168:171], v[126:129], v[208:211], v[168:171]
	s_waitcnt lgkmcnt(5)
	v_mfma_f32_16x16x32_f16 v[172:175], v[126:129], v[212:215], v[172:175]
	s_waitcnt lgkmcnt(4)
	v_mfma_f32_16x16x32_f16 v[50:53], v[126:129], v[216:219], v[50:53]
	s_waitcnt vmcnt(14)
	v_mfma_f32_16x16x32_f16 v[58:61], v[136:139], v[200:203], v[58:61]
	v_mfma_f32_16x16x32_f16 v[66:69], v[136:139], v[208:211], v[66:69]
	v_mfma_f32_16x16x32_f16 v[78:81], v[136:139], v[212:215], v[78:81]
	v_mfma_f32_16x16x32_f16 v[70:73], v[136:139], v[216:219], v[70:73]
	s_waitcnt vmcnt(13)
	v_mfma_f32_16x16x32_f16 v[54:57], v[184:187], v[200:203], v[54:57]
	v_mfma_f32_16x16x32_f16 v[74:77], v[184:187], v[208:211], v[74:77]
	v_mfma_f32_16x16x32_f16 v[82:85], v[184:187], v[212:215], v[82:85]
	v_mfma_f32_16x16x32_f16 v[62:65], v[184:187], v[216:219], v[62:65]
	s_waitcnt vmcnt(12)
	v_mfma_f32_16x16x32_f16 v[38:41], v[204:207], v[200:203], v[38:41]
	buffer_load_dwordx4 v[126:129], v147, s[16:19], s8 offen
	buffer_load_dwordx4 v[136:139], v148, s[16:19], s8 offen
	buffer_load_dwordx4 v[184:187], v149, s[16:19], s8 offen
	buffer_load_dwordx4 v[200:203], v150, s[16:19], s8 offen
	v_mfma_f32_16x16x32_f16 v[42:45], v[204:207], v[208:211], v[42:45]
	v_mfma_f32_16x16x32_f16 v[46:49], v[204:207], v[212:215], v[46:49]
	v_mfma_f32_16x16x32_f16 v[34:37], v[204:207], v[216:219], v[34:37]
	ds_read_b128 v[204:207], v111 offset:768
	ds_read_b128 v[208:211], v111 offset:17152
	ds_read_b128 v[212:215], v111 offset:33536
	ds_read_b128 v[216:219], v111 offset:49920
	s_add_i32 s8, s22, 0xfffe0000
	s_waitcnt vmcnt(15) lgkmcnt(7)
	v_mfma_f32_16x16x32_f16 v[164:167], v[94:97], v[176:179], v[164:167]
	s_waitcnt lgkmcnt(6)
	v_mfma_f32_16x16x32_f16 v[168:171], v[94:97], v[220:223], v[168:171]
	s_waitcnt vmcnt(14)
	v_mfma_f32_16x16x32_f16 v[58:61], v[122:125], v[176:179], v[58:61]
	v_mfma_f32_16x16x32_f16 v[66:69], v[122:125], v[220:223], v[66:69]
	s_waitcnt lgkmcnt(5)
	v_mfma_f32_16x16x32_f16 v[78:81], v[122:125], v[224:227], v[78:81]
	s_waitcnt lgkmcnt(4)
	v_mfma_f32_16x16x32_f16 v[70:73], v[122:125], v[228:231], v[70:73]
	s_waitcnt vmcnt(13)
	v_mfma_f32_16x16x32_f16 v[54:57], v[156:159], v[176:179], v[54:57]
	v_mfma_f32_16x16x32_f16 v[74:77], v[156:159], v[220:223], v[74:77]
	v_mfma_f32_16x16x32_f16 v[82:85], v[156:159], v[224:227], v[82:85]
	v_mfma_f32_16x16x32_f16 v[62:65], v[156:159], v[228:231], v[62:65]
	s_waitcnt vmcnt(12)
	v_mfma_f32_16x16x32_f16 v[38:41], v[180:183], v[176:179], v[38:41]
	v_mfma_f32_16x16x32_f16 v[42:45], v[180:183], v[220:223], v[42:45]
	buffer_load_dwordx4 v[122:125], v147, s[16:19], s8 offen
	buffer_load_dwordx4 v[156:159], v148, s[16:19], s8 offen
	buffer_load_dwordx4 v[176:179], v149, s[16:19], s8 offen
	buffer_load_dwordx4 v[220:223], v150, s[16:19], s8 offen
	v_mfma_f32_16x16x32_f16 v[50:53], v[94:97], v[228:231], v[50:53]
	v_mfma_f32_16x16x32_f16 v[46:49], v[180:183], v[224:227], v[46:49]
	v_mfma_f32_16x16x32_f16 v[34:37], v[180:183], v[228:231], v[34:37]
	v_mfma_f32_16x16x32_f16 v[172:175], v[94:97], v[224:227], v[172:175]
	ds_read_b128 v[94:97], v98 offset:768
	ds_read_b128 v[180:183], v98 offset:17152
	ds_read_b128 v[224:227], v98 offset:33536
	ds_read_b128 v[228:231], v98 offset:49920
	s_add_i32 s8, s22, 0xfffe8000
	s_waitcnt vmcnt(15) lgkmcnt(7)
	v_mfma_f32_16x16x32_f16 v[164:167], v[90:93], v[204:207], v[164:167]
	s_waitcnt lgkmcnt(6)
	v_mfma_f32_16x16x32_f16 v[168:171], v[90:93], v[208:211], v[168:171]
	s_waitcnt lgkmcnt(5)
	v_mfma_f32_16x16x32_f16 v[172:175], v[90:93], v[212:215], v[172:175]
	s_waitcnt lgkmcnt(4)
	v_mfma_f32_16x16x32_f16 v[90:93], v[90:93], v[216:219], v[50:53]
	s_waitcnt vmcnt(14)
	v_mfma_f32_16x16x32_f16 v[232:235], v[188:191], v[204:207], v[58:61]
	v_mfma_f32_16x16x32_f16 v[66:69], v[188:191], v[208:211], v[66:69]
	v_mfma_f32_16x16x32_f16 v[78:81], v[188:191], v[212:215], v[78:81]
	v_mfma_f32_16x16x32_f16 v[70:73], v[188:191], v[216:219], v[70:73]
	s_waitcnt vmcnt(13)
	v_mfma_f32_16x16x32_f16 v[188:191], v[192:195], v[204:207], v[54:57]
	v_mfma_f32_16x16x32_f16 v[74:77], v[192:195], v[208:211], v[74:77]
	v_mfma_f32_16x16x32_f16 v[82:85], v[192:195], v[212:215], v[82:85]
	v_mfma_f32_16x16x32_f16 v[62:65], v[192:195], v[216:219], v[62:65]
	s_waitcnt vmcnt(12)
	v_mfma_f32_16x16x32_f16 v[192:195], v[196:199], v[204:207], v[38:41]
	buffer_load_dwordx4 v[58:61], v147, s[16:19], s8 offen
	buffer_load_dwordx4 v[54:57], v148, s[16:19], s8 offen
	buffer_load_dwordx4 v[50:53], v149, s[16:19], s8 offen
	buffer_load_dwordx4 v[38:41], v150, s[16:19], s8 offen
	v_mfma_f32_16x16x32_f16 v[42:45], v[196:199], v[208:211], v[42:45]
	v_mfma_f32_16x16x32_f16 v[46:49], v[196:199], v[212:215], v[46:49]
	v_mfma_f32_16x16x32_f16 v[196:199], v[196:199], v[216:219], v[34:37]
	ds_read_b128 v[204:207], v99 offset:768
	ds_read_b128 v[208:211], v99 offset:17152
	ds_read_b128 v[212:215], v99 offset:33536
	ds_read_b128 v[216:219], v99 offset:49920
	s_add_i32 s8, s22, 0xffff0000
	s_waitcnt vmcnt(15) lgkmcnt(7)
	v_mfma_f32_16x16x32_f16 v[164:167], v[86:89], v[94:97], v[164:167]
	s_waitcnt lgkmcnt(6)
	v_mfma_f32_16x16x32_f16 v[168:171], v[86:89], v[180:183], v[168:171]
	s_waitcnt lgkmcnt(5)
	v_mfma_f32_16x16x32_f16 v[172:175], v[86:89], v[224:227], v[172:175]
	s_waitcnt lgkmcnt(4)
	v_mfma_f32_16x16x32_f16 v[86:89], v[86:89], v[228:231], v[90:93]
	s_waitcnt vmcnt(14)
	v_mfma_f32_16x16x32_f16 v[232:235], v[140:143], v[94:97], v[232:235]
	v_mfma_f32_16x16x32_f16 v[66:69], v[140:143], v[180:183], v[66:69]
	v_mfma_f32_16x16x32_f16 v[236:239], v[140:143], v[224:227], v[78:81]
	v_mfma_f32_16x16x32_f16 v[70:73], v[140:143], v[228:231], v[70:73]
	s_waitcnt vmcnt(13)
	v_mfma_f32_16x16x32_f16 v[140:143], v[152:155], v[94:97], v[188:191]
	v_mfma_f32_16x16x32_f16 v[74:77], v[152:155], v[180:183], v[74:77]
	v_mfma_f32_16x16x32_f16 v[82:85], v[152:155], v[224:227], v[82:85]
	v_mfma_f32_16x16x32_f16 v[62:65], v[152:155], v[228:231], v[62:65]
	s_waitcnt vmcnt(12)
	v_mfma_f32_16x16x32_f16 v[152:155], v[160:163], v[94:97], v[192:195]
	buffer_load_dwordx4 v[94:97], v147, s[16:19], s8 offen
	buffer_load_dwordx4 v[90:93], v148, s[16:19], s8 offen
	buffer_load_dwordx4 v[78:81], v149, s[16:19], s8 offen
	buffer_load_dwordx4 v[34:37], v150, s[16:19], s8 offen
	v_mfma_f32_16x16x32_f16 v[42:45], v[160:163], v[180:183], v[42:45]
	v_mfma_f32_16x16x32_f16 v[46:49], v[160:163], v[224:227], v[46:49]
	v_mfma_f32_16x16x32_f16 v[160:163], v[160:163], v[228:231], v[196:199]
	ds_read_b128 v[180:183], v100 offset:768
	ds_read_b128 v[188:191], v100 offset:17152
	ds_read_b128 v[192:195], v100 offset:33536
	ds_read_b128 v[196:199], v100 offset:49920
	s_add_i32 s8, s22, 0xffff8000
	s_waitcnt vmcnt(15) lgkmcnt(7)
	v_mfma_f32_16x16x32_f16 v[164:167], v[126:129], v[204:207], v[164:167]
	s_waitcnt lgkmcnt(6)
	v_mfma_f32_16x16x32_f16 v[168:171], v[126:129], v[208:211], v[168:171]
	s_waitcnt lgkmcnt(5)
	v_mfma_f32_16x16x32_f16 v[172:175], v[126:129], v[212:215], v[172:175]
	s_waitcnt lgkmcnt(4)
	v_mfma_f32_16x16x32_f16 v[86:89], v[126:129], v[216:219], v[86:89]
	s_waitcnt vmcnt(14)
	v_mfma_f32_16x16x32_f16 v[126:129], v[136:139], v[204:207], v[232:235]
	v_mfma_f32_16x16x32_f16 v[66:69], v[136:139], v[208:211], v[66:69]
	v_mfma_f32_16x16x32_f16 v[224:227], v[136:139], v[212:215], v[236:239]
	v_mfma_f32_16x16x32_f16 v[136:139], v[136:139], v[216:219], v[70:73]
	s_waitcnt vmcnt(13)
	v_mfma_f32_16x16x32_f16 v[140:143], v[184:187], v[204:207], v[140:143]
	v_mfma_f32_16x16x32_f16 v[74:77], v[184:187], v[208:211], v[74:77]
	v_mfma_f32_16x16x32_f16 v[228:231], v[184:187], v[212:215], v[82:85]
	v_mfma_f32_16x16x32_f16 v[184:187], v[184:187], v[216:219], v[62:65]
	s_waitcnt vmcnt(12)
	v_mfma_f32_16x16x32_f16 v[152:155], v[200:203], v[204:207], v[152:155]
	v_mfma_f32_16x16x32_f16 v[204:207], v[200:203], v[208:211], v[42:45]
	buffer_load_dwordx4 v[82:85], v147, s[16:19], s8 offen
	buffer_load_dwordx4 v[70:73], v148, s[16:19], s8 offen
	buffer_load_dwordx4 v[62:65], v149, s[16:19], s8 offen
	buffer_load_dwordx4 v[42:45], v150, s[16:19], s8 offen
	v_mfma_f32_16x16x32_f16 v[46:49], v[200:203], v[212:215], v[46:49]
	v_mfma_f32_16x16x32_f16 v[160:163], v[200:203], v[216:219], v[160:163]
	v_add_u32_e32 v0, 0x1ac00, v104
	ds_read_b128 v[240:243], v0
	ds_read_b128 v[244:247], v0 offset:16
	s_waitcnt vmcnt(12) lgkmcnt(5)
	v_mfma_f32_16x16x32_f16 v[164:167], v[122:125], v[180:183], v[164:167]
	v_mfma_f32_16x16x32_f16 v[126:129], v[156:159], v[180:183], v[126:129]
	v_mfma_f32_16x16x32_f16 v[140:143], v[176:179], v[180:183], v[140:143]
	v_mfma_f32_16x16x32_f16 v[152:155], v[220:223], v[180:183], v[152:155]
	s_waitcnt lgkmcnt(4)
	v_mfma_f32_16x16x32_f16 v[168:171], v[122:125], v[188:191], v[168:171]
	v_mfma_f32_16x16x32_f16 v[208:211], v[156:159], v[188:191], v[66:69]
	v_mfma_f32_16x16x32_f16 v[212:215], v[176:179], v[188:191], v[74:77]
	v_mfma_f32_16x16x32_f16 v[204:207], v[220:223], v[188:191], v[204:207]
	s_waitcnt lgkmcnt(3)
	v_mfma_f32_16x16x32_f16 v[172:175], v[122:125], v[192:195], v[172:175]
	v_cvt_pk_f16_f32 v232, v164, v165
	v_cvt_pk_f16_f32 v233, v166, v167
	v_pk_max_f16 v232, v232, 0
	v_pk_max_f16 v233, v233, 0
	v_mfma_f32_16x16x32_f16 v[224:227], v[156:159], v[192:195], v[224:227]
	v_cvt_pk_f16_f32 v234, v126, v127
	v_cvt_pk_f16_f32 v235, v128, v129
	v_pk_max_f16 v234, v234, 0
	v_pk_max_f16 v235, v235, 0
	v_mfma_f32_16x16x32_f16 v[228:231], v[176:179], v[192:195], v[228:231]
	v_cvt_pk_f16_f32 v236, v140, v141
	v_cvt_pk_f16_f32 v237, v142, v143
	v_pk_max_f16 v236, v236, 0
	v_pk_max_f16 v237, v237, 0
	v_mfma_f32_16x16x32_f16 v[216:219], v[220:223], v[192:195], v[46:49]
	v_cvt_pk_f16_f32 v238, v152, v153
	v_cvt_pk_f16_f32 v239, v154, v155
	v_pk_max_f16 v238, v238, 0
	v_pk_max_f16 v239, v239, 0
	s_waitcnt lgkmcnt(2)
	v_mfma_f32_16x16x32_f16 v[200:203], v[122:125], v[196:199], v[86:89]
	v_cvt_pk_f16_f32 v180, v168, v169
	v_cvt_pk_f16_f32 v181, v170, v171
	v_pk_max_f16 v180, v180, 0
	v_pk_max_f16 v181, v181, 0
	buffer_load_dwordx4 v[86:89], v147, s[16:19], s22 offen
	buffer_load_dwordx4 v[74:77], v148, s[16:19], s22 offen
	buffer_load_dwordx4 v[66:69], v149, s[16:19], s22 offen
	buffer_load_dwordx4 v[46:49], v150, s[16:19], s22 offen
	v_mfma_f32_16x16x32_f16 v[136:139], v[156:159], v[196:199], v[136:139]
	v_cvt_pk_f16_f32 v182, v208, v209
	v_cvt_pk_f16_f32 v183, v210, v211
	v_pk_max_f16 v182, v182, 0
	v_pk_max_f16 v183, v183, 0
	s_waitcnt lgkmcnt(1)
	v_mfma_f32_16x16x32_f16 v[252:255], v[240:243], v[232:235], 0
	v_mfma_f32_16x16x32_f16 v[184:187], v[176:179], v[196:199], v[184:187]
	v_cvt_pk_f16_f32 v188, v212, v213
	v_cvt_pk_f16_f32 v189, v214, v215
	v_pk_max_f16 v188, v188, 0
	v_pk_max_f16 v189, v189, 0
	s_waitcnt lgkmcnt(0)
	v_mfma_f32_16x16x32_f16 v[252:255], v[244:247], v[236:239], v[252:255]
	v_mfma_f32_16x16x32_f16 v[160:163], v[220:223], v[196:199], v[160:163]
	v_cvt_pk_f16_f32 v190, v204, v205
	v_cvt_pk_f16_f32 v191, v206, v207
	v_pk_max_f16 v190, v190, 0
	v_pk_max_f16 v191, v191, 0
	v_cvt_pk_f16_f32 v232, v172, v173
	v_cvt_pk_f16_f32 v233, v174, v175
	v_pk_max_f16 v232, v232, 0
	v_pk_max_f16 v233, v233, 0
	v_cvt_pk_f16_f32 v234, v224, v225
	v_cvt_pk_f16_f32 v235, v226, v227
	v_pk_max_f16 v234, v234, 0
	v_pk_max_f16 v235, v235, 0
	v_mfma_f32_16x16x32_f16 v[192:195], v[240:243], v[180:183], 0
	v_cvt_pk_f16_f32 v236, v228, v229
	v_cvt_pk_f16_f32 v237, v230, v231
	v_pk_max_f16 v236, v236, 0
	v_pk_max_f16 v237, v237, 0
	v_mfma_f32_16x16x32_f16 v[192:195], v[244:247], v[188:191], v[192:195]
	v_cvt_pk_f16_f32 v238, v216, v217
	v_cvt_pk_f16_f32 v239, v218, v219
	v_pk_max_f16 v238, v238, 0
	v_pk_max_f16 v239, v239, 0
	v_cvt_pk_f16_f32 v180, v200, v201
	v_cvt_pk_f16_f32 v181, v202, v203
	v_pk_max_f16 v180, v180, 0
	v_pk_max_f16 v181, v181, 0
	v_mfma_f32_16x16x32_f16 v[196:199], v[240:243], v[232:235], 0
	v_cvt_pk_f16_f32 v182, v136, v137
	v_cvt_pk_f16_f32 v183, v138, v139
	v_pk_max_f16 v182, v182, 0
	v_pk_max_f16 v183, v183, 0
	v_mfma_f32_16x16x32_f16 v[196:199], v[244:247], v[236:239], v[196:199]
	v_cvt_pk_f16_f32 v188, v184, v185
	v_cvt_pk_f16_f32 v189, v186, v187
	v_pk_max_f16 v188, v188, 0
	v_pk_max_f16 v189, v189, 0
	v_cvt_pk_f16_f32 v190, v160, v161
	v_cvt_pk_f16_f32 v191, v162, v163
	v_pk_max_f16 v190, v190, 0
	v_pk_max_f16 v191, v191, 0
	v_mfma_f32_16x16x32_f16 v[122:125], v[240:243], v[180:183], 0
	s_nop 0
	v_mfma_f32_16x16x32_f16 v[122:125], v[244:247], v[188:191], v[122:125]
	s_load_dword s30, s[12:13], 0x0
	v_cndmask_b32_e64 v0, v252, v192, s[2:3]
	v_cndmask_b32_e64 v0, v0, v196, s[0:1]
	s_waitcnt vmcnt(16)
	v_cndmask_b32_e64 v1, v30, v134, s[0:1]
	v_bfi_b32 v30, s10, v1, v30
	v_perm_b32 v1, v22, v134, s24
	v_cndmask_b32_e64 v22, v22, v1, s[0:1]
	v_bfi_b32 v1, s10, v135, v18
	v_perm_b32 v121, v10, v135, s24
	v_cndmask_b32_e64 v18, v18, v1, s[0:1]
	v_cndmask_b32_e64 v10, v10, v121, s[0:1]
	v_cndmask_b32_e64 v0, v0, v122, s[26:27]
	ds_write_b32 v112, v0
	s_waitcnt lgkmcnt(0)
	s_barrier
	ds_read_b128 v[232:235], v113
	s_add_i32 s31, s22, 0x68000
	buffer_load_dword v115, v116, s[16:19], s31 offen
	ds_read_b128 v[236:239], v113 offset:1024
	ds_read_u16 v248, v114
	ds_read_u16 v249, v114 offset:512
	ds_read_u16 v250, v114 offset:1024
	ds_read_u16 v251, v114 offset:1536
	s_and_b64 vcc, exec, s[4:5]
	s_waitcnt lgkmcnt(4)
	v_add_f32_e32 v0, v232, v233
	v_add_f32_e32 v1, v234, v235
	v_add_f32_e32 v121, v236, v237
	v_add_f32_e32 v144, v238, v239
	v_add_f32_e32 v0, v0, v1
	v_add_f32_e32 v121, v121, v144
	v_add_f32_e32 v0, v0, v121
	v_add_f32_e32 v0, s30, v0
	s_cbranch_vccnz .Lskip_out
	ds_write_b32 v106, v0
